# attention K/V sharing, 2 barriers per unit, the two units of a workgroup run half a unit apart (one extra barrier at entry for unit 1, at exit for unit 0)
# baseline (speedup 1.0000x reference)
.LBB0_427:
	v_or_b32_e32 v3, s3, v7
	v_lshlrev_b32_e32 v3, s1, v3
	v_add_u32_e32 v180, s42, v3
	s_movk_i32 s4, 0x1880
	v_mov_b64_e32 v[10:11], s[84:85]
	v_mad_i64_i32 v[10:11], s[4:5], v180, s4, v[10:11]
	s_lshl_b32 s4, s2, 1
	s_mov_b32 s5, 0
	v_lshl_add_u64 v[10:11], v[10:11], 0, s[4:5]
	v_lshlrev_b32_e32 v12, 4, v6
	v_mov_b32_e32 v13, 0
	v_lshl_add_u64 v[10:11], v[10:11], 0, v[12:13]
	global_load_dwordx4 v[146:149], v[10:11], off offset:96
	global_load_dwordx4 v[150:153], v[10:11], off offset:64
	global_load_dwordx4 v[154:157], v[10:11], off offset:32
	global_load_dwordx4 v[158:161], v[10:11], off
	s_lshl_b32 s81, 1, s1
	s_lshl_b32 s1, 0xffffff80, s1
	s_waitcnt vmcnt(0)
	s_add_i32 s82, s42, s1
	v_lshlrev_b32_e32 v2, 4, v2
	s_movk_i32 s1, 0x1000
	v_add3_u32 v182, v1, v2, s1
	s_movk_i32 s16, 0x1880
	v_and_b32_e32 v100, 63, v0
	v_lshrrev_b32_e32 v101, 3, v100
	v_and_b32_e32 v104, 7, v100
	v_xor_b32_e32 v104, v104, v101
	v_lshlrev_b32_e32 v104, 4, v104
	s_lshl_b32 s10, s88, 7
	s_add_u32 s10, s10, 0x800
	v_add_u32_e32 v104, s10, v104
	v_mov_b32_e32 v105, 0
	v_lshl_add_u64 v[106:107], s[84:85], 0, v[104:105]
	s_bfe_u32 s11, s75, 0x2000c
	s_and_b32 s12, s75, 0xffff0000
	s_add_u32 s12, s12, 0x8000
	s_add_u32 s13, s11, 1
	s_lshl_b32 s10, s13, 5
	v_add_u32_e32 v102, s10, v101
	s_lshl_b32 s10, s13, 12
	s_add_u32 s10, s10, s12
	v_mul_lo_u32 v103, v102, s81
	v_add_u32_e32 v103, s82, v103
	v_max_i32_e32 v103, 0, v103
	s_mov_b32 m0, s10
	v_mad_u64_u32 v[108:109], vcc, v103, s16, v[106:107]
	global_load_lds_dwordx4 v[108:109], off
	v_add_u32_e32 v102, 8, v102
	v_mul_lo_u32 v103, v102, s81
	v_add_u32_e32 v103, s82, v103
	v_max_i32_e32 v103, 0, v103
	s_add_u32 m0, s10, 0x400
	v_mad_u64_u32 v[108:109], vcc, v103, s16, v[106:107]
	global_load_lds_dwordx4 v[108:109], off
	v_add_u32_e32 v102, 8, v102
	v_mul_lo_u32 v103, v102, s81
	v_add_u32_e32 v103, s82, v103
	v_max_i32_e32 v103, 0, v103
	s_add_u32 m0, s10, 0x800
	v_mad_u64_u32 v[108:109], vcc, v103, s16, v[106:107]
	global_load_lds_dwordx4 v[108:109], off
	v_add_u32_e32 v102, 8, v102
	v_mul_lo_u32 v103, v102, s81
	v_add_u32_e32 v103, s82, v103
	v_max_i32_e32 v103, 0, v103
	s_add_u32 m0, s10, 0xc00
	v_mad_u64_u32 v[108:109], vcc, v103, s16, v[106:107]
	global_load_lds_dwordx4 v[108:109], off
	s_add_u32 s13, s11, 4
	s_cmp_eq_u32 s11, 0
	s_cselect_b32 s13, 0, s13
	s_lshl_b32 s10, s13, 5
	v_add_u32_e32 v102, s10, v101
	s_lshl_b32 s10, s13, 12
	s_add_u32 s10, s10, s12
	v_mul_lo_u32 v103, v102, s81
	v_add_u32_e32 v103, s82, v103
	v_max_i32_e32 v103, 0, v103
	s_mov_b32 m0, s10
	v_mad_u64_u32 v[108:109], vcc, v103, s16, v[106:107]
	global_load_lds_dwordx4 v[108:109], off
	v_add_u32_e32 v102, 8, v102
	v_mul_lo_u32 v103, v102, s81
	v_add_u32_e32 v103, s82, v103
	v_max_i32_e32 v103, 0, v103
	s_add_u32 m0, s10, 0x400
	v_mad_u64_u32 v[108:109], vcc, v103, s16, v[106:107]
	global_load_lds_dwordx4 v[108:109], off
	v_add_u32_e32 v102, 8, v102
	v_mul_lo_u32 v103, v102, s81
	v_add_u32_e32 v103, s82, v103
	v_max_i32_e32 v103, 0, v103
	s_add_u32 m0, s10, 0x800
	v_mad_u64_u32 v[108:109], vcc, v103, s16, v[106:107]
	global_load_lds_dwordx4 v[108:109], off
	v_add_u32_e32 v102, 8, v102
	v_mul_lo_u32 v103, v102, s81
	v_add_u32_e32 v103, s82, v103
	v_max_i32_e32 v103, 0, v103
	s_add_u32 m0, s10, 0xc00
	v_mad_u64_u32 v[108:109], vcc, v103, s16, v[106:107]
	global_load_lds_dwordx4 v[108:109], off
	v_and_b32_e32 v100, 63, v0
	v_lshrrev_b32_e32 v101, 3, v100
	v_and_b32_e32 v104, 7, v100
	v_lshlrev_b32_e32 v104, 4, v104
	s_lshl_b32 s10, s88, 7
	s_add_u32 s10, s10, 0x1000
	v_add_u32_e32 v104, s10, v104
	v_mov_b32_e32 v105, 0
	v_lshl_add_u64 v[106:107], s[84:85], 0, v[104:105]
	s_bfe_u32 s11, s75, 0x2000c
	s_and_b32 s12, s75, 0xffff0000
	s_add_u32 s13, s11, 1
	s_lshl_b32 s10, s13, 5
	v_add_u32_e32 v102, s10, v101
	s_lshl_b32 s10, s13, 12
	s_add_u32 s10, s10, s12
	v_mul_lo_u32 v103, v102, s81
	v_add_u32_e32 v103, s82, v103
	v_max_i32_e32 v103, 0, v103
	s_mov_b32 m0, s10
	v_mad_u64_u32 v[108:109], vcc, v103, s16, v[106:107]
	global_load_lds_dwordx4 v[108:109], off
	v_add_u32_e32 v102, 8, v102
	v_mul_lo_u32 v103, v102, s81
	v_add_u32_e32 v103, s82, v103
	v_max_i32_e32 v103, 0, v103
	s_add_u32 m0, s10, 0x400
	v_mad_u64_u32 v[108:109], vcc, v103, s16, v[106:107]
	global_load_lds_dwordx4 v[108:109], off
	v_add_u32_e32 v102, 8, v102
	v_mul_lo_u32 v103, v102, s81
	v_add_u32_e32 v103, s82, v103
	v_max_i32_e32 v103, 0, v103
	s_add_u32 m0, s10, 0x800
	v_mad_u64_u32 v[108:109], vcc, v103, s16, v[106:107]
	global_load_lds_dwordx4 v[108:109], off
	v_add_u32_e32 v102, 8, v102
	v_mul_lo_u32 v103, v102, s81
	v_add_u32_e32 v103, s82, v103
	v_max_i32_e32 v103, 0, v103
	s_add_u32 m0, s10, 0xc00
	v_mad_u64_u32 v[108:109], vcc, v103, s16, v[106:107]
	global_load_lds_dwordx4 v[108:109], off
	s_add_u32 s13, s11, 4
	s_cmp_eq_u32 s11, 0
	s_cselect_b32 s13, 0, s13
	s_lshl_b32 s10, s13, 5
	v_add_u32_e32 v102, s10, v101
	s_lshl_b32 s10, s13, 12
	s_add_u32 s10, s10, s12
	v_mul_lo_u32 v103, v102, s81
	v_add_u32_e32 v103, s82, v103
	v_max_i32_e32 v103, 0, v103
	s_mov_b32 m0, s10
	v_mad_u64_u32 v[108:109], vcc, v103, s16, v[106:107]
	global_load_lds_dwordx4 v[108:109], off
	v_add_u32_e32 v102, 8, v102
	v_mul_lo_u32 v103, v102, s81
	v_add_u32_e32 v103, s82, v103
	v_max_i32_e32 v103, 0, v103
	s_add_u32 m0, s10, 0x400
	v_mad_u64_u32 v[108:109], vcc, v103, s16, v[106:107]
	global_load_lds_dwordx4 v[108:109], off
	v_add_u32_e32 v102, 8, v102
	v_mul_lo_u32 v103, v102, s81
	v_add_u32_e32 v103, s82, v103
	v_max_i32_e32 v103, 0, v103
	s_add_u32 m0, s10, 0x800
	v_mad_u64_u32 v[108:109], vcc, v103, s16, v[106:107]
	global_load_lds_dwordx4 v[108:109], off
	v_add_u32_e32 v102, 8, v102
	v_mul_lo_u32 v103, v102, s81
	v_add_u32_e32 v103, s82, v103
	v_max_i32_e32 v103, 0, v103
	s_add_u32 m0, s10, 0xc00
	v_mad_u64_u32 v[108:109], vcc, v103, s16, v[106:107]
	global_load_lds_dwordx4 v[108:109], off
	s_waitcnt vmcnt(0)
	s_barrier
	v_readlane_b32 s10, v254, 14
	s_cmp_eq_u32 s10, 0
	s_cbranch_scc1 .Latt_off0
	s_barrier
.Latt_off0:
	s_andn2_b64 vcc, exec, s[8:9]
	s_cbranch_vccz .LBB0_429
	s_branch .LBB0_492

.LBB0_491:
	v_readlane_b32 s0, v254, 14
	s_cmp_eq_u32 s0, 1
	s_cbranch_scc1 .Latt_off1
	s_barrier
